# in-proj GEMM epilogues specialised: plain bf16-store and e4m3 gate-store fast paths without the per-group scaled/unscaled pk_mul+cndmask select (old path kept for the two scaled NA-q tiles); on top of
# speedup vs baseline: 1.0031x; 1.0031x over previous
.LBB0_293:
	s_lshl_b32 s0, s0, 8
	v_mbcnt_lo_u32_b32 v144, -1, 0
	v_mbcnt_hi_u32_b32 v144, -1, v144
	s_add_i32 s0, s0, s54
	v_and_or_b32 v150, v144, 15, s0
	v_ashrrev_i32_e32 v144, 1, v144
	s_lshl_b32 s0, s4, 8
	v_and_b32_e32 v144, -8, v144
	s_or_b32 s0, s0, s55
	v_add_u32_e32 v144, s0, v144
	v_mov_b64_e32 v[146:147], s[8:9]
	v_ashrrev_i32_e32 v145, 31, v144
	v_mad_i64_i32 v[160:161], vcc, v150, s88, v[146:147]
	v_lshl_add_u64 v[160:161], v[144:145], 1, v[160:161]
	v_cvt_pk_bf16_f32 v152, v130, v131
	v_cvt_pk_bf16_f32 v153, v132, v133
	v_cvt_pk_bf16_f32 v154, v126, v127
	v_cvt_pk_bf16_f32 v155, v128, v129
	global_store_dwordx4 v[160:161], v[152:155], off
	v_cvt_pk_bf16_f32 v156, v122, v123
	v_cvt_pk_bf16_f32 v157, v124, v125
	v_cvt_pk_bf16_f32 v158, v118, v119
	v_cvt_pk_bf16_f32 v159, v120, v121
	global_store_dwordx4 v[160:161], v[156:159], off offset:256
	v_add_u32_e32 v151, 16, v150
	v_mad_i64_i32 v[160:161], vcc, v151, s88, v[146:147]
	v_lshl_add_u64 v[160:161], v[144:145], 1, v[160:161]
	v_cvt_pk_bf16_f32 v152, v114, v115
	v_cvt_pk_bf16_f32 v153, v116, v117
	v_cvt_pk_bf16_f32 v154, v110, v111
	v_cvt_pk_bf16_f32 v155, v112, v113
	global_store_dwordx4 v[160:161], v[152:155], off
	v_cvt_pk_bf16_f32 v156, v106, v107
	v_cvt_pk_bf16_f32 v157, v108, v109
	v_cvt_pk_bf16_f32 v158, v102, v103
	v_cvt_pk_bf16_f32 v159, v104, v105
	global_store_dwordx4 v[160:161], v[156:159], off offset:256
	v_add_u32_e32 v151, 32, v150
	v_mad_i64_i32 v[160:161], vcc, v151, s88, v[146:147]
	v_lshl_add_u64 v[160:161], v[144:145], 1, v[160:161]
	v_cvt_pk_bf16_f32 v152, v98, v99
	v_cvt_pk_bf16_f32 v153, v100, v101
	v_cvt_pk_bf16_f32 v154, v94, v95
	v_cvt_pk_bf16_f32 v155, v96, v97
	global_store_dwordx4 v[160:161], v[152:155], off
	v_cvt_pk_bf16_f32 v156, v90, v91
	v_cvt_pk_bf16_f32 v157, v92, v93
	v_cvt_pk_bf16_f32 v158, v86, v87
	v_cvt_pk_bf16_f32 v159, v88, v89
	global_store_dwordx4 v[160:161], v[156:159], off offset:256
	v_add_u32_e32 v151, 48, v150
	v_mad_i64_i32 v[160:161], vcc, v151, s88, v[146:147]
	v_lshl_add_u64 v[160:161], v[144:145], 1, v[160:161]
	v_cvt_pk_bf16_f32 v152, v82, v83
	v_cvt_pk_bf16_f32 v153, v84, v85
	v_cvt_pk_bf16_f32 v154, v78, v79
	v_cvt_pk_bf16_f32 v155, v80, v81
	global_store_dwordx4 v[160:161], v[152:155], off
	v_cvt_pk_bf16_f32 v156, v74, v75
	v_cvt_pk_bf16_f32 v157, v76, v77
	v_cvt_pk_bf16_f32 v158, v70, v71
	v_cvt_pk_bf16_f32 v159, v72, v73
	global_store_dwordx4 v[160:161], v[156:159], off offset:256
	v_add_u32_e32 v151, 128, v150
	v_mad_i64_i32 v[160:161], vcc, v151, s88, v[146:147]
	v_lshl_add_u64 v[160:161], v[144:145], 1, v[160:161]
	v_cvt_pk_bf16_f32 v152, v66, v67
	v_cvt_pk_bf16_f32 v153, v68, v69
	v_cvt_pk_bf16_f32 v154, v62, v63
	v_cvt_pk_bf16_f32 v155, v64, v65
	global_store_dwordx4 v[160:161], v[152:155], off
	v_cvt_pk_bf16_f32 v156, v58, v59
	v_cvt_pk_bf16_f32 v157, v60, v61
	v_cvt_pk_bf16_f32 v158, v54, v55
	v_cvt_pk_bf16_f32 v159, v56, v57
	global_store_dwordx4 v[160:161], v[156:159], off offset:256
	v_add_u32_e32 v151, 144, v150
	v_mad_i64_i32 v[160:161], vcc, v151, s88, v[146:147]
	v_lshl_add_u64 v[160:161], v[144:145], 1, v[160:161]
	v_cvt_pk_bf16_f32 v152, v50, v51
	v_cvt_pk_bf16_f32 v153, v52, v53
	v_cvt_pk_bf16_f32 v154, v46, v47
	v_cvt_pk_bf16_f32 v155, v48, v49
	global_store_dwordx4 v[160:161], v[152:155], off
	v_cvt_pk_bf16_f32 v156, v42, v43
	v_cvt_pk_bf16_f32 v157, v44, v45
	v_cvt_pk_bf16_f32 v158, v38, v39
	v_cvt_pk_bf16_f32 v159, v40, v41
	global_store_dwordx4 v[160:161], v[156:159], off offset:256
	v_add_u32_e32 v151, 160, v150
	v_mad_i64_i32 v[160:161], vcc, v151, s88, v[146:147]
	v_lshl_add_u64 v[160:161], v[144:145], 1, v[160:161]
	v_cvt_pk_bf16_f32 v152, v34, v35
	v_cvt_pk_bf16_f32 v153, v36, v37
	v_cvt_pk_bf16_f32 v154, v30, v31
	v_cvt_pk_bf16_f32 v155, v32, v33
	global_store_dwordx4 v[160:161], v[152:155], off
	v_cvt_pk_bf16_f32 v156, v26, v27
	v_cvt_pk_bf16_f32 v157, v28, v29
	v_cvt_pk_bf16_f32 v158, v22, v23
	v_cvt_pk_bf16_f32 v159, v24, v25
	global_store_dwordx4 v[160:161], v[156:159], off offset:256
	v_add_u32_e32 v151, 176, v150
	v_mad_i64_i32 v[160:161], vcc, v151, s88, v[146:147]
	v_lshl_add_u64 v[160:161], v[144:145], 1, v[160:161]
	v_cvt_pk_bf16_f32 v152, v18, v19
	v_cvt_pk_bf16_f32 v153, v20, v21
	v_cvt_pk_bf16_f32 v154, v14, v15
	v_cvt_pk_bf16_f32 v155, v16, v17
	global_store_dwordx4 v[160:161], v[152:155], off
	v_cvt_pk_bf16_f32 v156, v10, v11
	v_cvt_pk_bf16_f32 v157, v12, v13
	v_cvt_pk_bf16_f32 v158, v6, v7
	v_cvt_pk_bf16_f32 v159, v8, v9
	global_store_dwordx4 v[160:161], v[156:159], off offset:256
	s_andn2_b64 vcc, exec, s[38:39]
	s_mov_b64 s[0:1], -1
	s_cbranch_vccnz .LBB0_285
	s_branch .LBB0_358

.LBB0_391:
	s_lshl_b32 s0, s0, 8
	s_nop 15
	s_nop 15
	s_and_b32 vcc_lo, s4, -2
	s_cmp_eq_u32 vcc_lo, 6
	s_cbranch_scc1 .Lepi_old_ip8
	s_cmp_gt_i32 s4, 14
	s_cbranch_scc1 .Lepi_gate_ip8
	v_mbcnt_lo_u32_b32 v2, -1, 0
	v_mbcnt_hi_u32_b32 v2, -1, v2
	s_add_i32 s0, s0, s81
	v_and_or_b32 v8, v2, 15, s0
	v_ashrrev_i32_e32 v2, 1, v2
	s_lshl_b32 s0, s4, 8
	v_and_b32_e32 v2, -8, v2
	s_or_b32 s0, s0, s6
	v_add_u32_e32 v2, s0, v2
	v_mov_b64_e32 v[4:5], s[8:9]
	v_ashrrev_i32_e32 v3, 31, v2
	v_mad_i64_i32 v[6:7], vcc, v8, s88, v[4:5]
	v_lshl_add_u64 v[6:7], v[2:3], 1, v[6:7]
	v_cvt_pk_bf16_f32 v10, v158, v159
	v_cvt_pk_bf16_f32 v11, v160, v161
	v_cvt_pk_bf16_f32 v12, v154, v155
	v_cvt_pk_bf16_f32 v13, v156, v157
	global_store_dwordx4 v[6:7], v[10:13], off
	v_cvt_pk_bf16_f32 v14, v126, v127
	v_cvt_pk_bf16_f32 v15, v128, v129
	v_cvt_pk_bf16_f32 v16, v122, v123
	v_cvt_pk_bf16_f32 v17, v124, v125
	global_store_dwordx4 v[6:7], v[14:17], off offset:256
	v_add_u32_e32 v9, 16, v8
	v_mad_i64_i32 v[6:7], vcc, v9, s88, v[4:5]
	v_lshl_add_u64 v[6:7], v[2:3], 1, v[6:7]
	v_cvt_pk_bf16_f32 v10, v150, v151
	v_cvt_pk_bf16_f32 v11, v152, v153
	v_cvt_pk_bf16_f32 v12, v146, v147
	v_cvt_pk_bf16_f32 v13, v148, v149
	global_store_dwordx4 v[6:7], v[10:13], off
	v_cvt_pk_bf16_f32 v14, v118, v119
	v_cvt_pk_bf16_f32 v15, v120, v121
	v_cvt_pk_bf16_f32 v16, v114, v115
	v_cvt_pk_bf16_f32 v17, v116, v117
	global_store_dwordx4 v[6:7], v[14:17], off offset:256
	v_add_u32_e32 v9, 32, v8
	v_mad_i64_i32 v[6:7], vcc, v9, s88, v[4:5]
	v_lshl_add_u64 v[6:7], v[2:3], 1, v[6:7]
	v_cvt_pk_bf16_f32 v10, v142, v143
	v_cvt_pk_bf16_f32 v11, v144, v145
	v_cvt_pk_bf16_f32 v12, v138, v139
	v_cvt_pk_bf16_f32 v13, v140, v141
	global_store_dwordx4 v[6:7], v[10:13], off
	v_cvt_pk_bf16_f32 v14, v110, v111
	v_cvt_pk_bf16_f32 v15, v112, v113
	v_cvt_pk_bf16_f32 v16, v106, v107
	v_cvt_pk_bf16_f32 v17, v108, v109
	global_store_dwordx4 v[6:7], v[14:17], off offset:256
	v_add_u32_e32 v9, 48, v8
	v_mad_i64_i32 v[6:7], vcc, v9, s88, v[4:5]
	v_lshl_add_u64 v[6:7], v[2:3], 1, v[6:7]
	v_cvt_pk_bf16_f32 v10, v134, v135
	v_cvt_pk_bf16_f32 v11, v136, v137
	v_cvt_pk_bf16_f32 v12, v130, v131
	v_cvt_pk_bf16_f32 v13, v132, v133
	global_store_dwordx4 v[6:7], v[10:13], off
	v_cvt_pk_bf16_f32 v14, v102, v103
	v_cvt_pk_bf16_f32 v15, v104, v105
	v_cvt_pk_bf16_f32 v16, v98, v99
	v_cvt_pk_bf16_f32 v17, v100, v101
	global_store_dwordx4 v[6:7], v[14:17], off offset:256
	v_add_u32_e32 v9, 128, v8
	v_mad_i64_i32 v[6:7], vcc, v9, s88, v[4:5]
	v_lshl_add_u64 v[6:7], v[2:3], 1, v[6:7]
	v_cvt_pk_bf16_f32 v10, v94, v95
	v_cvt_pk_bf16_f32 v11, v96, v97
	v_cvt_pk_bf16_f32 v12, v90, v91
	v_cvt_pk_bf16_f32 v13, v92, v93
	global_store_dwordx4 v[6:7], v[10:13], off
	v_cvt_pk_bf16_f32 v14, v62, v63
	v_cvt_pk_bf16_f32 v15, v64, v65
	v_cvt_pk_bf16_f32 v16, v58, v59
	v_cvt_pk_bf16_f32 v17, v60, v61
	global_store_dwordx4 v[6:7], v[14:17], off offset:256
	v_add_u32_e32 v9, 144, v8
	v_mad_i64_i32 v[6:7], vcc, v9, s88, v[4:5]
	v_lshl_add_u64 v[6:7], v[2:3], 1, v[6:7]
	v_cvt_pk_bf16_f32 v10, v86, v87
	v_cvt_pk_bf16_f32 v11, v88, v89
	v_cvt_pk_bf16_f32 v12, v82, v83
	v_cvt_pk_bf16_f32 v13, v84, v85
	global_store_dwordx4 v[6:7], v[10:13], off
	v_cvt_pk_bf16_f32 v14, v54, v55
	v_cvt_pk_bf16_f32 v15, v56, v57
	v_cvt_pk_bf16_f32 v16, v50, v51
	v_cvt_pk_bf16_f32 v17, v52, v53
	global_store_dwordx4 v[6:7], v[14:17], off offset:256
	v_add_u32_e32 v9, 160, v8
	v_mad_i64_i32 v[6:7], vcc, v9, s88, v[4:5]
	v_lshl_add_u64 v[6:7], v[2:3], 1, v[6:7]
	v_cvt_pk_bf16_f32 v10, v78, v79
	v_cvt_pk_bf16_f32 v11, v80, v81
	v_cvt_pk_bf16_f32 v12, v74, v75
	v_cvt_pk_bf16_f32 v13, v76, v77
	global_store_dwordx4 v[6:7], v[10:13], off
	v_cvt_pk_bf16_f32 v14, v46, v47
	v_cvt_pk_bf16_f32 v15, v48, v49
	v_cvt_pk_bf16_f32 v16, v42, v43
	v_cvt_pk_bf16_f32 v17, v44, v45
	global_store_dwordx4 v[6:7], v[14:17], off offset:256
	v_add_u32_e32 v9, 176, v8
	v_mad_i64_i32 v[6:7], vcc, v9, s88, v[4:5]
	v_lshl_add_u64 v[6:7], v[2:3], 1, v[6:7]
	v_cvt_pk_bf16_f32 v10, v70, v71
	v_cvt_pk_bf16_f32 v11, v72, v73
	v_cvt_pk_bf16_f32 v12, v66, v67
	v_cvt_pk_bf16_f32 v13, v68, v69
	global_store_dwordx4 v[6:7], v[10:13], off
	v_cvt_pk_bf16_f32 v14, v38, v39
	v_cvt_pk_bf16_f32 v15, v40, v41
	v_cvt_pk_bf16_f32 v16, v34, v35
	v_cvt_pk_bf16_f32 v17, v36, v37
	global_store_dwordx4 v[6:7], v[14:17], off offset:256
	s_andn2_b64 vcc, exec, s[42:43]
	s_mov_b64 s[0:1], -1
	s_cbranch_vccnz .LBB0_373
	s_branch .LBB0_456
.Lepi_gate_ip8:
	v_mbcnt_lo_u32_b32 v2, -1, 0
	v_mbcnt_hi_u32_b32 v2, -1, v2
	s_add_i32 s0, s0, s81
	v_and_or_b32 v8, v2, 15, s0
	v_ashrrev_i32_e32 v2, 1, v2
	s_lshl_b32 s0, s4, 8
	v_and_b32_e32 v2, -8, v2
	s_or_b32 s0, s0, s6
	v_add_u32_e32 v2, s0, v2
	v_mov_b64_e32 v[4:5], s[8:9]
	v_ashrrev_i32_e32 v3, 31, v2
	v_mad_i64_i32 v[6:7], vcc, v8, s88, v[4:5]
	v_lshl_add_u64 v[6:7], v[6:7], 0, v[2:3]
	v_mul_f32_e32 v18, 0xbfb8aa3b, v158
	v_mul_f32_e32 v19, 0xbfb8aa3b, v159
	v_mul_f32_e32 v20, 0xbfb8aa3b, v160
	v_mul_f32_e32 v21, 0xbfb8aa3b, v161
	v_mul_f32_e32 v22, 0xbfb8aa3b, v154
	v_mul_f32_e32 v23, 0xbfb8aa3b, v155
	v_mul_f32_e32 v24, 0xbfb8aa3b, v156
	v_mul_f32_e32 v25, 0xbfb8aa3b, v157
	v_min_f32_e32 v18, 0x410c0000, v18
	v_min_f32_e32 v19, 0x410c0000, v19
	v_min_f32_e32 v20, 0x410c0000, v20
	v_min_f32_e32 v21, 0x410c0000, v21
	v_min_f32_e32 v22, 0x410c0000, v22
	v_min_f32_e32 v23, 0x410c0000, v23
	v_min_f32_e32 v24, 0x410c0000, v24
	v_min_f32_e32 v25, 0x410c0000, v25
	v_exp_f32_e32 v18, v18
	v_exp_f32_e32 v19, v19
	v_exp_f32_e32 v20, v20
	v_exp_f32_e32 v21, v21
	v_exp_f32_e32 v22, v22
	v_exp_f32_e32 v23, v23
	v_exp_f32_e32 v24, v24
	v_exp_f32_e32 v25, v25
	v_cvt_pk_fp8_f32 v10, v18, v19
	v_cvt_pk_fp8_f32 v11, v22, v23
	v_cvt_pk_fp8_f32 v10, v20, v21 op_sel:[0,0,1]
	v_cvt_pk_fp8_f32 v11, v24, v25 op_sel:[0,0,1]
	s_nop 0
	global_store_dwordx2 v[6:7], v[10:11], off offset:3840
	v_mul_f32_e32 v18, 0xbfb8aa3b, v126
	v_mul_f32_e32 v19, 0xbfb8aa3b, v127
	v_mul_f32_e32 v20, 0xbfb8aa3b, v128
	v_mul_f32_e32 v21, 0xbfb8aa3b, v129
	v_mul_f32_e32 v22, 0xbfb8aa3b, v122
	v_mul_f32_e32 v23, 0xbfb8aa3b, v123
	v_mul_f32_e32 v24, 0xbfb8aa3b, v124
	v_mul_f32_e32 v25, 0xbfb8aa3b, v125
	v_min_f32_e32 v18, 0x410c0000, v18
	v_min_f32_e32 v19, 0x410c0000, v19
	v_min_f32_e32 v20, 0x410c0000, v20
	v_min_f32_e32 v21, 0x410c0000, v21
	v_min_f32_e32 v22, 0x410c0000, v22
	v_min_f32_e32 v23, 0x410c0000, v23
	v_min_f32_e32 v24, 0x410c0000, v24
	v_min_f32_e32 v25, 0x410c0000, v25
	v_exp_f32_e32 v18, v18
	v_exp_f32_e32 v19, v19
	v_exp_f32_e32 v20, v20
	v_exp_f32_e32 v21, v21
	v_exp_f32_e32 v22, v22
	v_exp_f32_e32 v23, v23
	v_exp_f32_e32 v24, v24
	v_exp_f32_e32 v25, v25
	v_cvt_pk_fp8_f32 v14, v18, v19
	v_cvt_pk_fp8_f32 v15, v22, v23
	v_cvt_pk_fp8_f32 v14, v20, v21 op_sel:[0,0,1]
	v_cvt_pk_fp8_f32 v15, v24, v25 op_sel:[0,0,1]
	s_nop 0
	global_store_dwordx2 v[6:7], v[14:15], off offset:3968
	v_add_u32_e32 v9, 16, v8
	v_mad_i64_i32 v[6:7], vcc, v9, s88, v[4:5]
	v_lshl_add_u64 v[6:7], v[6:7], 0, v[2:3]
	v_mul_f32_e32 v18, 0xbfb8aa3b, v150
	v_mul_f32_e32 v19, 0xbfb8aa3b, v151
	v_mul_f32_e32 v20, 0xbfb8aa3b, v152
	v_mul_f32_e32 v21, 0xbfb8aa3b, v153
	v_mul_f32_e32 v22, 0xbfb8aa3b, v146
	v_mul_f32_e32 v23, 0xbfb8aa3b, v147
	v_mul_f32_e32 v24, 0xbfb8aa3b, v148
	v_mul_f32_e32 v25, 0xbfb8aa3b, v149
	v_min_f32_e32 v18, 0x410c0000, v18
	v_min_f32_e32 v19, 0x410c0000, v19
	v_min_f32_e32 v20, 0x410c0000, v20
	v_min_f32_e32 v21, 0x410c0000, v21
	v_min_f32_e32 v22, 0x410c0000, v22
	v_min_f32_e32 v23, 0x410c0000, v23
	v_min_f32_e32 v24, 0x410c0000, v24
	v_min_f32_e32 v25, 0x410c0000, v25
	v_exp_f32_e32 v18, v18
	v_exp_f32_e32 v19, v19
	v_exp_f32_e32 v20, v20
	v_exp_f32_e32 v21, v21
	v_exp_f32_e32 v22, v22
	v_exp_f32_e32 v23, v23
	v_exp_f32_e32 v24, v24
	v_exp_f32_e32 v25, v25
	v_cvt_pk_fp8_f32 v10, v18, v19
	v_cvt_pk_fp8_f32 v11, v22, v23
	v_cvt_pk_fp8_f32 v10, v20, v21 op_sel:[0,0,1]
	v_cvt_pk_fp8_f32 v11, v24, v25 op_sel:[0,0,1]
	s_nop 0
	global_store_dwordx2 v[6:7], v[10:11], off offset:3840
	v_mul_f32_e32 v18, 0xbfb8aa3b, v118
	v_mul_f32_e32 v19, 0xbfb8aa3b, v119
	v_mul_f32_e32 v20, 0xbfb8aa3b, v120
	v_mul_f32_e32 v21, 0xbfb8aa3b, v121
	v_mul_f32_e32 v22, 0xbfb8aa3b, v114
	v_mul_f32_e32 v23, 0xbfb8aa3b, v115
	v_mul_f32_e32 v24, 0xbfb8aa3b, v116
	v_mul_f32_e32 v25, 0xbfb8aa3b, v117
	v_min_f32_e32 v18, 0x410c0000, v18
	v_min_f32_e32 v19, 0x410c0000, v19
	v_min_f32_e32 v20, 0x410c0000, v20
	v_min_f32_e32 v21, 0x410c0000, v21
	v_min_f32_e32 v22, 0x410c0000, v22
	v_min_f32_e32 v23, 0x410c0000, v23
	v_min_f32_e32 v24, 0x410c0000, v24
	v_min_f32_e32 v25, 0x410c0000, v25
	v_exp_f32_e32 v18, v18
	v_exp_f32_e32 v19, v19
	v_exp_f32_e32 v20, v20
	v_exp_f32_e32 v21, v21
	v_exp_f32_e32 v22, v22
	v_exp_f32_e32 v23, v23
	v_exp_f32_e32 v24, v24
	v_exp_f32_e32 v25, v25
	v_cvt_pk_fp8_f32 v14, v18, v19
	v_cvt_pk_fp8_f32 v15, v22, v23
	v_cvt_pk_fp8_f32 v14, v20, v21 op_sel:[0,0,1]
	v_cvt_pk_fp8_f32 v15, v24, v25 op_sel:[0,0,1]
	s_nop 0
	global_store_dwordx2 v[6:7], v[14:15], off offset:3968
	v_add_u32_e32 v9, 32, v8
	v_mad_i64_i32 v[6:7], vcc, v9, s88, v[4:5]
	v_lshl_add_u64 v[6:7], v[6:7], 0, v[2:3]
	v_mul_f32_e32 v18, 0xbfb8aa3b, v142
	v_mul_f32_e32 v19, 0xbfb8aa3b, v143
	v_mul_f32_e32 v20, 0xbfb8aa3b, v144
	v_mul_f32_e32 v21, 0xbfb8aa3b, v145
	v_mul_f32_e32 v22, 0xbfb8aa3b, v138
	v_mul_f32_e32 v23, 0xbfb8aa3b, v139
	v_mul_f32_e32 v24, 0xbfb8aa3b, v140
	v_mul_f32_e32 v25, 0xbfb8aa3b, v141
	v_min_f32_e32 v18, 0x410c0000, v18
	v_min_f32_e32 v19, 0x410c0000, v19
	v_min_f32_e32 v20, 0x410c0000, v20
	v_min_f32_e32 v21, 0x410c0000, v21
	v_min_f32_e32 v22, 0x410c0000, v22
	v_min_f32_e32 v23, 0x410c0000, v23
	v_min_f32_e32 v24, 0x410c0000, v24
	v_min_f32_e32 v25, 0x410c0000, v25
	v_exp_f32_e32 v18, v18
	v_exp_f32_e32 v19, v19
	v_exp_f32_e32 v20, v20
	v_exp_f32_e32 v21, v21
	v_exp_f32_e32 v22, v22
	v_exp_f32_e32 v23, v23
	v_exp_f32_e32 v24, v24
	v_exp_f32_e32 v25, v25
	v_cvt_pk_fp8_f32 v10, v18, v19
	v_cvt_pk_fp8_f32 v11, v22, v23
	v_cvt_pk_fp8_f32 v10, v20, v21 op_sel:[0,0,1]
	v_cvt_pk_fp8_f32 v11, v24, v25 op_sel:[0,0,1]
	s_nop 0
	global_store_dwordx2 v[6:7], v[10:11], off offset:3840
	v_mul_f32_e32 v18, 0xbfb8aa3b, v110
	v_mul_f32_e32 v19, 0xbfb8aa3b, v111
	v_mul_f32_e32 v20, 0xbfb8aa3b, v112
	v_mul_f32_e32 v21, 0xbfb8aa3b, v113
	v_mul_f32_e32 v22, 0xbfb8aa3b, v106
	v_mul_f32_e32 v23, 0xbfb8aa3b, v107
	v_mul_f32_e32 v24, 0xbfb8aa3b, v108
	v_mul_f32_e32 v25, 0xbfb8aa3b, v109
	v_min_f32_e32 v18, 0x410c0000, v18
	v_min_f32_e32 v19, 0x410c0000, v19
	v_min_f32_e32 v20, 0x410c0000, v20
	v_min_f32_e32 v21, 0x410c0000, v21
	v_min_f32_e32 v22, 0x410c0000, v22
	v_min_f32_e32 v23, 0x410c0000, v23
	v_min_f32_e32 v24, 0x410c0000, v24
	v_min_f32_e32 v25, 0x410c0000, v25
	v_exp_f32_e32 v18, v18
	v_exp_f32_e32 v19, v19
	v_exp_f32_e32 v20, v20
	v_exp_f32_e32 v21, v21
	v_exp_f32_e32 v22, v22
	v_exp_f32_e32 v23, v23
	v_exp_f32_e32 v24, v24
	v_exp_f32_e32 v25, v25
	v_cvt_pk_fp8_f32 v14, v18, v19
	v_cvt_pk_fp8_f32 v15, v22, v23
	v_cvt_pk_fp8_f32 v14, v20, v21 op_sel:[0,0,1]
	v_cvt_pk_fp8_f32 v15, v24, v25 op_sel:[0,0,1]
	s_nop 0
	global_store_dwordx2 v[6:7], v[14:15], off offset:3968
	v_add_u32_e32 v9, 48, v8
	v_mad_i64_i32 v[6:7], vcc, v9, s88, v[4:5]
	v_lshl_add_u64 v[6:7], v[6:7], 0, v[2:3]
	v_mul_f32_e32 v18, 0xbfb8aa3b, v134
	v_mul_f32_e32 v19, 0xbfb8aa3b, v135
	v_mul_f32_e32 v20, 0xbfb8aa3b, v136
	v_mul_f32_e32 v21, 0xbfb8aa3b, v137
	v_mul_f32_e32 v22, 0xbfb8aa3b, v130
	v_mul_f32_e32 v23, 0xbfb8aa3b, v131
	v_mul_f32_e32 v24, 0xbfb8aa3b, v132
	v_mul_f32_e32 v25, 0xbfb8aa3b, v133
	v_min_f32_e32 v18, 0x410c0000, v18
	v_min_f32_e32 v19, 0x410c0000, v19
	v_min_f32_e32 v20, 0x410c0000, v20
	v_min_f32_e32 v21, 0x410c0000, v21
	v_min_f32_e32 v22, 0x410c0000, v22
	v_min_f32_e32 v23, 0x410c0000, v23
	v_min_f32_e32 v24, 0x410c0000, v24
	v_min_f32_e32 v25, 0x410c0000, v25
	v_exp_f32_e32 v18, v18
	v_exp_f32_e32 v19, v19
	v_exp_f32_e32 v20, v20
	v_exp_f32_e32 v21, v21
	v_exp_f32_e32 v22, v22
	v_exp_f32_e32 v23, v23
	v_exp_f32_e32 v24, v24
	v_exp_f32_e32 v25, v25
	v_cvt_pk_fp8_f32 v10, v18, v19
	v_cvt_pk_fp8_f32 v11, v22, v23
	v_cvt_pk_fp8_f32 v10, v20, v21 op_sel:[0,0,1]
	v_cvt_pk_fp8_f32 v11, v24, v25 op_sel:[0,0,1]
	s_nop 0
	global_store_dwordx2 v[6:7], v[10:11], off offset:3840
	v_mul_f32_e32 v18, 0xbfb8aa3b, v102
	v_mul_f32_e32 v19, 0xbfb8aa3b, v103
	v_mul_f32_e32 v20, 0xbfb8aa3b, v104
	v_mul_f32_e32 v21, 0xbfb8aa3b, v105
	v_mul_f32_e32 v22, 0xbfb8aa3b, v98
	v_mul_f32_e32 v23, 0xbfb8aa3b, v99
	v_mul_f32_e32 v24, 0xbfb8aa3b, v100
	v_mul_f32_e32 v25, 0xbfb8aa3b, v101
	v_min_f32_e32 v18, 0x410c0000, v18
	v_min_f32_e32 v19, 0x410c0000, v19
	v_min_f32_e32 v20, 0x410c0000, v20
	v_min_f32_e32 v21, 0x410c0000, v21
	v_min_f32_e32 v22, 0x410c0000, v22
	v_min_f32_e32 v23, 0x410c0000, v23
	v_min_f32_e32 v24, 0x410c0000, v24
	v_min_f32_e32 v25, 0x410c0000, v25
	v_exp_f32_e32 v18, v18
	v_exp_f32_e32 v19, v19
	v_exp_f32_e32 v20, v20
	v_exp_f32_e32 v21, v21
	v_exp_f32_e32 v22, v22
	v_exp_f32_e32 v23, v23
	v_exp_f32_e32 v24, v24
	v_exp_f32_e32 v25, v25
	v_cvt_pk_fp8_f32 v14, v18, v19
	v_cvt_pk_fp8_f32 v15, v22, v23
	v_cvt_pk_fp8_f32 v14, v20, v21 op_sel:[0,0,1]
	v_cvt_pk_fp8_f32 v15, v24, v25 op_sel:[0,0,1]
	s_nop 0
	global_store_dwordx2 v[6:7], v[14:15], off offset:3968
	v_add_u32_e32 v9, 128, v8
	v_mad_i64_i32 v[6:7], vcc, v9, s88, v[4:5]
	v_lshl_add_u64 v[6:7], v[6:7], 0, v[2:3]
	v_mul_f32_e32 v18, 0xbfb8aa3b, v94
	v_mul_f32_e32 v19, 0xbfb8aa3b, v95
	v_mul_f32_e32 v20, 0xbfb8aa3b, v96
	v_mul_f32_e32 v21, 0xbfb8aa3b, v97
	v_mul_f32_e32 v22, 0xbfb8aa3b, v90
	v_mul_f32_e32 v23, 0xbfb8aa3b, v91
	v_mul_f32_e32 v24, 0xbfb8aa3b, v92
	v_mul_f32_e32 v25, 0xbfb8aa3b, v93
	v_min_f32_e32 v18, 0x410c0000, v18
	v_min_f32_e32 v19, 0x410c0000, v19
	v_min_f32_e32 v20, 0x410c0000, v20
	v_min_f32_e32 v21, 0x410c0000, v21
	v_min_f32_e32 v22, 0x410c0000, v22
	v_min_f32_e32 v23, 0x410c0000, v23
	v_min_f32_e32 v24, 0x410c0000, v24
	v_min_f32_e32 v25, 0x410c0000, v25
	v_exp_f32_e32 v18, v18
	v_exp_f32_e32 v19, v19
	v_exp_f32_e32 v20, v20
	v_exp_f32_e32 v21, v21
	v_exp_f32_e32 v22, v22
	v_exp_f32_e32 v23, v23
	v_exp_f32_e32 v24, v24
	v_exp_f32_e32 v25, v25
	v_cvt_pk_fp8_f32 v10, v18, v19
	v_cvt_pk_fp8_f32 v11, v22, v23
	v_cvt_pk_fp8_f32 v10, v20, v21 op_sel:[0,0,1]
	v_cvt_pk_fp8_f32 v11, v24, v25 op_sel:[0,0,1]
	s_nop 0
	global_store_dwordx2 v[6:7], v[10:11], off offset:3840
	v_mul_f32_e32 v18, 0xbfb8aa3b, v62
	v_mul_f32_e32 v19, 0xbfb8aa3b, v63
	v_mul_f32_e32 v20, 0xbfb8aa3b, v64
	v_mul_f32_e32 v21, 0xbfb8aa3b, v65
	v_mul_f32_e32 v22, 0xbfb8aa3b, v58
	v_mul_f32_e32 v23, 0xbfb8aa3b, v59
	v_mul_f32_e32 v24, 0xbfb8aa3b, v60
	v_mul_f32_e32 v25, 0xbfb8aa3b, v61
	v_min_f32_e32 v18, 0x410c0000, v18
	v_min_f32_e32 v19, 0x410c0000, v19
	v_min_f32_e32 v20, 0x410c0000, v20
	v_min_f32_e32 v21, 0x410c0000, v21
	v_min_f32_e32 v22, 0x410c0000, v22
	v_min_f32_e32 v23, 0x410c0000, v23
	v_min_f32_e32 v24, 0x410c0000, v24
	v_min_f32_e32 v25, 0x410c0000, v25
	v_exp_f32_e32 v18, v18
	v_exp_f32_e32 v19, v19
	v_exp_f32_e32 v20, v20
	v_exp_f32_e32 v21, v21
	v_exp_f32_e32 v22, v22
	v_exp_f32_e32 v23, v23
	v_exp_f32_e32 v24, v24
	v_exp_f32_e32 v25, v25
	v_cvt_pk_fp8_f32 v14, v18, v19
	v_cvt_pk_fp8_f32 v15, v22, v23
	v_cvt_pk_fp8_f32 v14, v20, v21 op_sel:[0,0,1]
	v_cvt_pk_fp8_f32 v15, v24, v25 op_sel:[0,0,1]
	s_nop 0
	global_store_dwordx2 v[6:7], v[14:15], off offset:3968
	v_add_u32_e32 v9, 144, v8
	v_mad_i64_i32 v[6:7], vcc, v9, s88, v[4:5]
	v_lshl_add_u64 v[6:7], v[6:7], 0, v[2:3]
	v_mul_f32_e32 v18, 0xbfb8aa3b, v86
	v_mul_f32_e32 v19, 0xbfb8aa3b, v87
	v_mul_f32_e32 v20, 0xbfb8aa3b, v88
	v_mul_f32_e32 v21, 0xbfb8aa3b, v89
	v_mul_f32_e32 v22, 0xbfb8aa3b, v82
	v_mul_f32_e32 v23, 0xbfb8aa3b, v83
	v_mul_f32_e32 v24, 0xbfb8aa3b, v84
	v_mul_f32_e32 v25, 0xbfb8aa3b, v85
	v_min_f32_e32 v18, 0x410c0000, v18
	v_min_f32_e32 v19, 0x410c0000, v19
	v_min_f32_e32 v20, 0x410c0000, v20
	v_min_f32_e32 v21, 0x410c0000, v21
	v_min_f32_e32 v22, 0x410c0000, v22
	v_min_f32_e32 v23, 0x410c0000, v23
	v_min_f32_e32 v24, 0x410c0000, v24
	v_min_f32_e32 v25, 0x410c0000, v25
	v_exp_f32_e32 v18, v18
	v_exp_f32_e32 v19, v19
	v_exp_f32_e32 v20, v20
	v_exp_f32_e32 v21, v21
	v_exp_f32_e32 v22, v22
	v_exp_f32_e32 v23, v23
	v_exp_f32_e32 v24, v24
	v_exp_f32_e32 v25, v25
	v_cvt_pk_fp8_f32 v10, v18, v19
	v_cvt_pk_fp8_f32 v11, v22, v23
	v_cvt_pk_fp8_f32 v10, v20, v21 op_sel:[0,0,1]
	v_cvt_pk_fp8_f32 v11, v24, v25 op_sel:[0,0,1]
	s_nop 0
	global_store_dwordx2 v[6:7], v[10:11], off offset:3840
	v_mul_f32_e32 v18, 0xbfb8aa3b, v54
	v_mul_f32_e32 v19, 0xbfb8aa3b, v55
	v_mul_f32_e32 v20, 0xbfb8aa3b, v56
	v_mul_f32_e32 v21, 0xbfb8aa3b, v57
	v_mul_f32_e32 v22, 0xbfb8aa3b, v50
	v_mul_f32_e32 v23, 0xbfb8aa3b, v51
	v_mul_f32_e32 v24, 0xbfb8aa3b, v52
	v_mul_f32_e32 v25, 0xbfb8aa3b, v53
	v_min_f32_e32 v18, 0x410c0000, v18
	v_min_f32_e32 v19, 0x410c0000, v19
	v_min_f32_e32 v20, 0x410c0000, v20
	v_min_f32_e32 v21, 0x410c0000, v21
	v_min_f32_e32 v22, 0x410c0000, v22
	v_min_f32_e32 v23, 0x410c0000, v23
	v_min_f32_e32 v24, 0x410c0000, v24
	v_min_f32_e32 v25, 0x410c0000, v25
	v_exp_f32_e32 v18, v18
	v_exp_f32_e32 v19, v19
	v_exp_f32_e32 v20, v20
	v_exp_f32_e32 v21, v21
	v_exp_f32_e32 v22, v22
	v_exp_f32_e32 v23, v23
	v_exp_f32_e32 v24, v24
	v_exp_f32_e32 v25, v25
	v_cvt_pk_fp8_f32 v14, v18, v19
	v_cvt_pk_fp8_f32 v15, v22, v23
	v_cvt_pk_fp8_f32 v14, v20, v21 op_sel:[0,0,1]
	v_cvt_pk_fp8_f32 v15, v24, v25 op_sel:[0,0,1]
	s_nop 0
	global_store_dwordx2 v[6:7], v[14:15], off offset:3968
	v_add_u32_e32 v9, 160, v8
	v_mad_i64_i32 v[6:7], vcc, v9, s88, v[4:5]
	v_lshl_add_u64 v[6:7], v[6:7], 0, v[2:3]
	v_mul_f32_e32 v18, 0xbfb8aa3b, v78
	v_mul_f32_e32 v19, 0xbfb8aa3b, v79
	v_mul_f32_e32 v20, 0xbfb8aa3b, v80
	v_mul_f32_e32 v21, 0xbfb8aa3b, v81
	v_mul_f32_e32 v22, 0xbfb8aa3b, v74
	v_mul_f32_e32 v23, 0xbfb8aa3b, v75
	v_mul_f32_e32 v24, 0xbfb8aa3b, v76
	v_mul_f32_e32 v25, 0xbfb8aa3b, v77
	v_min_f32_e32 v18, 0x410c0000, v18
	v_min_f32_e32 v19, 0x410c0000, v19
	v_min_f32_e32 v20, 0x410c0000, v20
	v_min_f32_e32 v21, 0x410c0000, v21
	v_min_f32_e32 v22, 0x410c0000, v22
	v_min_f32_e32 v23, 0x410c0000, v23
	v_min_f32_e32 v24, 0x410c0000, v24
	v_min_f32_e32 v25, 0x410c0000, v25
	v_exp_f32_e32 v18, v18
	v_exp_f32_e32 v19, v19
	v_exp_f32_e32 v20, v20
	v_exp_f32_e32 v21, v21
	v_exp_f32_e32 v22, v22
	v_exp_f32_e32 v23, v23
	v_exp_f32_e32 v24, v24
	v_exp_f32_e32 v25, v25
	v_cvt_pk_fp8_f32 v10, v18, v19
	v_cvt_pk_fp8_f32 v11, v22, v23
	v_cvt_pk_fp8_f32 v10, v20, v21 op_sel:[0,0,1]
	v_cvt_pk_fp8_f32 v11, v24, v25 op_sel:[0,0,1]
	s_nop 0
	global_store_dwordx2 v[6:7], v[10:11], off offset:3840
	v_mul_f32_e32 v18, 0xbfb8aa3b, v46
	v_mul_f32_e32 v19, 0xbfb8aa3b, v47
	v_mul_f32_e32 v20, 0xbfb8aa3b, v48
	v_mul_f32_e32 v21, 0xbfb8aa3b, v49
	v_mul_f32_e32 v22, 0xbfb8aa3b, v42
	v_mul_f32_e32 v23, 0xbfb8aa3b, v43
	v_mul_f32_e32 v24, 0xbfb8aa3b, v44
	v_mul_f32_e32 v25, 0xbfb8aa3b, v45
	v_min_f32_e32 v18, 0x410c0000, v18
	v_min_f32_e32 v19, 0x410c0000, v19
	v_min_f32_e32 v20, 0x410c0000, v20
	v_min_f32_e32 v21, 0x410c0000, v21
	v_min_f32_e32 v22, 0x410c0000, v22
	v_min_f32_e32 v23, 0x410c0000, v23
	v_min_f32_e32 v24, 0x410c0000, v24
	v_min_f32_e32 v25, 0x410c0000, v25
	v_exp_f32_e32 v18, v18
	v_exp_f32_e32 v19, v19
	v_exp_f32_e32 v20, v20
	v_exp_f32_e32 v21, v21
	v_exp_f32_e32 v22, v22
	v_exp_f32_e32 v23, v23
	v_exp_f32_e32 v24, v24
	v_exp_f32_e32 v25, v25
	v_cvt_pk_fp8_f32 v14, v18, v19
	v_cvt_pk_fp8_f32 v15, v22, v23
	v_cvt_pk_fp8_f32 v14, v20, v21 op_sel:[0,0,1]
	v_cvt_pk_fp8_f32 v15, v24, v25 op_sel:[0,0,1]
	s_nop 0
	global_store_dwordx2 v[6:7], v[14:15], off offset:3968
	v_add_u32_e32 v9, 176, v8
	v_mad_i64_i32 v[6:7], vcc, v9, s88, v[4:5]
	v_lshl_add_u64 v[6:7], v[6:7], 0, v[2:3]
	v_mul_f32_e32 v18, 0xbfb8aa3b, v70
	v_mul_f32_e32 v19, 0xbfb8aa3b, v71
	v_mul_f32_e32 v20, 0xbfb8aa3b, v72
	v_mul_f32_e32 v21, 0xbfb8aa3b, v73
	v_mul_f32_e32 v22, 0xbfb8aa3b, v66
	v_mul_f32_e32 v23, 0xbfb8aa3b, v67
	v_mul_f32_e32 v24, 0xbfb8aa3b, v68
	v_mul_f32_e32 v25, 0xbfb8aa3b, v69
	v_min_f32_e32 v18, 0x410c0000, v18
	v_min_f32_e32 v19, 0x410c0000, v19
	v_min_f32_e32 v20, 0x410c0000, v20
	v_min_f32_e32 v21, 0x410c0000, v21
	v_min_f32_e32 v22, 0x410c0000, v22
	v_min_f32_e32 v23, 0x410c0000, v23
	v_min_f32_e32 v24, 0x410c0000, v24
	v_min_f32_e32 v25, 0x410c0000, v25
	v_exp_f32_e32 v18, v18
	v_exp_f32_e32 v19, v19
	v_exp_f32_e32 v20, v20
	v_exp_f32_e32 v21, v21
	v_exp_f32_e32 v22, v22
	v_exp_f32_e32 v23, v23
	v_exp_f32_e32 v24, v24
	v_exp_f32_e32 v25, v25
	v_cvt_pk_fp8_f32 v10, v18, v19
	v_cvt_pk_fp8_f32 v11, v22, v23
	v_cvt_pk_fp8_f32 v10, v20, v21 op_sel:[0,0,1]
	v_cvt_pk_fp8_f32 v11, v24, v25 op_sel:[0,0,1]
	s_nop 0
	global_store_dwordx2 v[6:7], v[10:11], off offset:3840
	v_mul_f32_e32 v18, 0xbfb8aa3b, v38
	v_mul_f32_e32 v19, 0xbfb8aa3b, v39
	v_mul_f32_e32 v20, 0xbfb8aa3b, v40
	v_mul_f32_e32 v21, 0xbfb8aa3b, v41
	v_mul_f32_e32 v22, 0xbfb8aa3b, v34
	v_mul_f32_e32 v23, 0xbfb8aa3b, v35
	v_mul_f32_e32 v24, 0xbfb8aa3b, v36
	v_mul_f32_e32 v25, 0xbfb8aa3b, v37
	v_min_f32_e32 v18, 0x410c0000, v18
	v_min_f32_e32 v19, 0x410c0000, v19
	v_min_f32_e32 v20, 0x410c0000, v20
	v_min_f32_e32 v21, 0x410c0000, v21
	v_min_f32_e32 v22, 0x410c0000, v22
	v_min_f32_e32 v23, 0x410c0000, v23
	v_min_f32_e32 v24, 0x410c0000, v24
	v_min_f32_e32 v25, 0x410c0000, v25
	v_exp_f32_e32 v18, v18
	v_exp_f32_e32 v19, v19
	v_exp_f32_e32 v20, v20
	v_exp_f32_e32 v21, v21
	v_exp_f32_e32 v22, v22
	v_exp_f32_e32 v23, v23
	v_exp_f32_e32 v24, v24
	v_exp_f32_e32 v25, v25
	v_cvt_pk_fp8_f32 v14, v18, v19
	v_cvt_pk_fp8_f32 v15, v22, v23
	v_cvt_pk_fp8_f32 v14, v20, v21 op_sel:[0,0,1]
	v_cvt_pk_fp8_f32 v15, v24, v25 op_sel:[0,0,1]
	s_nop 0
	global_store_dwordx2 v[6:7], v[14:15], off offset:3968
	s_andn2_b64 vcc, exec, s[42:43]
	s_mov_b64 s[0:1], -1
	s_cbranch_vccnz .LBB0_373
	s_branch .LBB0_456
.Lepi_old_ip8:
	v_mbcnt_lo_u32_b32 v2, -1, 0
	v_mbcnt_hi_u32_b32 v2, -1, v2
	s_add_i32 s0, s0, s81
	v_and_or_b32 v8, v2, 15, s0
	v_ashrrev_i32_e32 v2, 1, v2
	s_lshl_b32 s0, s4, 8
	v_and_b32_e32 v2, -8, v2
	s_or_b32 s0, s0, s6
	v_add_u32_e32 v2, s0, v2
	s_and_b32 s0, s4, -2
	v_mov_b64_e32 v[4:5], s[8:9]
	s_cmp_eq_u32 s0, 6
	v_mad_i64_i32 v[6:7], s[0:1], v8, s88, v[4:5]
	v_ashrrev_i32_e32 v3, 31, v2
	v_pk_mul_f32 v[4:5], v[160:161], s[14:15] op_sel_hi:[1,0]
	v_pk_mul_f32 v[10:11], v[158:159], s[14:15] op_sel_hi:[1,0]
	v_pk_mul_f32 v[18:19], v[156:157], s[14:15] op_sel_hi:[1,0]
	v_pk_mul_f32 v[20:21], v[154:155], s[14:15] op_sel_hi:[1,0]
	s_cselect_b64 s[0:1], -1, 0
	s_cmp_gt_i32 s4, 14
	v_cndmask_b32_e64 v14, v159, v11, s[0:1]
	v_cndmask_b32_e64 v16, v158, v10, s[0:1]
	v_cndmask_b32_e64 v12, v161, v5, s[0:1]
	v_cndmask_b32_e64 v15, v160, v4, s[0:1]
	v_cndmask_b32_e64 v10, v155, v21, s[0:1]
	v_cndmask_b32_e64 v13, v154, v20, s[0:1]
	v_cndmask_b32_e64 v9, v157, v19, s[0:1]
	v_cndmask_b32_e64 v11, v156, v18, s[0:1]
	s_cselect_b64 s[44:45], -1, 0
	s_cmp_lt_i32 s4, 15
	s_mov_b64 s[4:5], -1
	v_lshl_add_u64 v[4:5], v[6:7], 0, v[2:3]
	s_cbranch_scc1 .LBB0_393
	v_mul_f32_e32 v18, 0xbfb8aa3b, v13
	v_min_f32_e32 v18, 0x410c0000, v18
	v_exp_f32_e32 v20, v18
	v_mul_f32_e32 v18, 0xbfb8aa3b, v14
	v_min_f32_e32 v18, 0x410c0000, v18
	v_exp_f32_e32 v19, v18
	v_mul_f32_e32 v18, 0xbfb8aa3b, v10
	v_min_f32_e32 v18, 0x410c0000, v18
	v_exp_f32_e32 v21, v18
	v_mul_f32_e32 v18, 0xbfb8aa3b, v15
	v_min_f32_e32 v18, 0x410c0000, v18
	v_exp_f32_e32 v22, v18
	v_mul_f32_e32 v18, 0xbfb8aa3b, v11
	v_mul_f32_e32 v17, 0xbfb8aa3b, v16
	v_min_f32_e32 v18, 0x410c0000, v18
	v_min_f32_e32 v17, 0x410c0000, v17
	v_exp_f32_e32 v23, v18
	v_mul_f32_e32 v18, 0xbfb8aa3b, v12
	v_exp_f32_e32 v17, v17
	v_min_f32_e32 v18, 0x410c0000, v18
	v_exp_f32_e32 v24, v18
	v_mul_f32_e32 v18, 0xbfb8aa3b, v9
	v_min_f32_e32 v18, 0x410c0000, v18
	v_exp_f32_e32 v25, v18
	v_mov_b32_e32 v18, v1
	v_cvt_pk_fp8_f32 v18, v17, v19
	v_mov_b32_e32 v19, v1
	v_cvt_pk_fp8_f32 v19, v20, v21
	s_mov_b64 s[4:5], 0
	v_cvt_pk_fp8_f32 v18, v22, v24 op_sel:[0,0,1]
	v_cvt_pk_fp8_f32 v19, v23, v25 op_sel:[0,0,1]
	global_store_dwordx2 v[4:5], v[18:19], off offset:3840
